# helper workgroups: the 8-unit workgroups of the busy XCD groups convert 17% of the layer-1 weights after E1 and 8% after E2 (their XCD links are otherwise idle), the lightly loaded XCD groups the rema
# baseline (speedup 1.0000x reference)
; #define KIN(i) ((const float*)(GAS const float*)karg()[i])
; #define WSP(type, off) ((type*)(KWS() + (off)))
; #define CBID() (LOCAL_OK() ? ((bid & 7) * 32 + (bid >> 3)) : bid)
; __global__ void __launch_bounds__(NWAVES * 64, 2) mk_fwd(Args args) {
;     ...
;         const float* x = KIN(0); const float* norm_mix_g = KIN(2); const float* mod = WSP(float, WS_MOD); bf16_t* xn = WSP(bf16_t, WS_XN);
;         for (int w0 = (CBID() * 8 + wave) * 32; w0 < T; w0 += G * 8 * 32) {
;             const float* mb = mod + (size_t)(w0 >> 12) * 6144;
;             ModV mv; mod_load(mv, norm_mix_g, mb + 0, mb + 1024, lane);
;             RowV ring[4];
; #pragma unroll
;             for (int d = 0; d < 4; ++d) row_load(ring[d], x + (size_t)(w0 + d) * D, lane);
.LBB0_739:
	s_cmp_eq_u32 s99, 1
	s_cbranch_scc1 .Lseam5_go
	s_cmp_eq_u32 s99, 2
	s_cbranch_scc1 .Lq_done
	s_cmp_eq_u32 s99, 5
	s_cbranch_scc1 .LslotA_ret
	s_cmpk_lg_i32 s33, 0x100
	s_cselect_b64 s[0:1], -1, 0
	v_writelane_b32 v251, s0, 9
	s_and_b32 s54, s50, 0xe0
	s_mov_b64 s[8:9], s[78:79]
	v_writelane_b32 v251, s1, 10
	s_lshr_b32 s0, s83, 3
	s_add_i32 s6, s54, s0
	s_cmpk_eq_i32 s33, 0x100
	s_cselect_b64 s[2:3], -1, 0
	s_and_b64 s[0:1], s[2:3], exec
	s_cselect_b32 s0, s6, s83
	s_lshl_b32 s0, s0, 8
	s_lshl_b32 s96, s85, 5
	s_add_i32 s6, s0, s96
	s_lshl_b32 s0, s33, 8
	v_writelane_b32 v251, s0, 11
	s_cmp_gt_i32 s6, 0xffff
	s_mov_b64 s[10:11], s[78:79]
	v_writelane_b32 v251, s1, 12
	s_mov_b64 s[0:1], s[78:79]
	s_mov_b64 s[12:13], s[78:79]
	s_cbranch_scc1 .LBB0_754
	s_load_dwordx2 s[14:15], s[10:11], 0xa0
	s_load_dwordx2 s[16:17], s[0:1], 0x0
	s_load_dwordx2 s[20:21], s[8:9], 0x10
	s_load_dwordx2 s[22:23], s[12:13], 0xa0
	v_ashrrev_i32_e32 v133, 31, v132
	s_waitcnt vmcnt(15)
	v_lshlrev_b64 v[0:1], 2, v[132:133]
	s_waitcnt lgkmcnt(0)
	s_add_u32 s18, s14, 0x100000
	v_lshl_add_u64 v[96:97], s[20:21], 0, v[0:1]
	v_lshl_add_u64 v[98:99], s[16:17], 0, v[0:1]
	v_lshlrev_b64 v[0:1], 1, v[132:133]
	s_addc_u32 s19, s15, 0
	v_lshl_add_u64 v[2:3], s[22:23], 0, v[0:1]
	s_mov_b64 s[0:1], 0x10000000
	s_ashr_i32 s7, s6, 31
	v_lshl_add_u64 v[100:101], v[2:3], 0, s[0:1]
	s_lshl_b64 s[0:1], s[6:7], 11
	s_add_u32 s0, s22, s0
	s_addc_u32 s1, s23, s1
	v_lshl_add_u64 v[0:1], s[0:1], 0, v[0:1]
	s_mov_b64 s[0:1], 0x10000400
	v_lshl_add_u64 v[102:103], v[0:1], 0, s[0:1]
	v_readlane_b32 s0, v251, 11
	v_readlane_b32 s1, v251, 12
	s_mov_b32 s8, s0
	s_ashr_i32 s9, s0, 31
	v_writelane_b32 v251, s0, 11
	s_lshl_b64 s[8:9], s[8:9], 11
	s_mov_b64 s[10:11], 0x1000
	v_mov_b32_e32 v122, 0x358637bd
	s_mov_b64 s[12:13], 0x2000
	v_writelane_b32 v251, s1, 12
	s_branch .LBB0_742

;     __device__ bool next(int i, Unit& u) const {
;         const long L = (long)i * G + c; int wgid;
;         if (aligned) {
;             const int ng = (nM + WGM - 1) / WGM, gq = ng / NXCD, gr = ng % NXCD, xcd = (int)(L % NXCD); const long off = L / NXCD;
;             const int g0 = xcd * gq + (xcd < gr ? xcd : gr), g1 = g0 + gq + (xcd < gr ? 1 : 0);
;             const long w = (long)g0 * (WGM * 4) + off, wend = (long)g1 * (WGM * 4) < nwg ? (long)g1 * (WGM * 4) : nwg;
;             if (w >= wend) return false;
;             wgid = (int)w;
; __global__ void __launch_bounds__(NWAVES * 64, 2) mk_fwd(Args args) {
;     ...
;         {
;             const int step = G * NWAVES; int it0 = CONV_EARLY + bid * NWAVES + wave;
;             ConvDesc dA, dB; f32x4 vA[16], vB[16];
;             if (it0 < NCONV_ITEMS) { CONV_DECODE(dA, it0); conv_load(vA, dA, lane); }
; #pragma unroll 1
;             for (; it0 < NCONV_ITEMS; it0 += 2 * step) {
;                 const bool hasB = it0 + step < NCONV_ITEMS, hasA2 = it0 + 2 * step < NCONV_ITEMS;
;                 if (hasB) { CONV_DECODE(dB, it0 + step); conv_load(vB, dB, lane); }
;                 conv_process(vA, dA, scr, lane);
;                 if (hasA2) { CONV_DECODE(dA, it0 + 2 * step); conv_load(vA, dA, lane); }
;                 if (hasB) conv_process(vB, dB, scr, lane);
;             }
.LBB0_1541:
	v_mov_b32_e32 v252, 0x27c80
	ds_read_b32 v252, v252
	s_waitcnt lgkmcnt(0)
	v_readfirstlane_b32 s100, v252
	s_nop 1
	s_lshr_b32 s100, s100, 8
	s_add_i32 s100, s100, 3
	s_lshr_b32 s100, s100, 2
	s_and_b32 s100, s100, 7
	s_cmp_eq_u32 s100, 0
	s_cbranch_scc1 .LslotA_skip
	s_cmp_ge_u32 s100, 6
	s_cbranch_scc1 .LslotA_skip
	s_and_b32 s98, s83, 7
	s_cmp_ge_u32 s98, s100
	s_cbranch_scc1 .LslotA_skip
	s_lshr_b32 s101, s83, 3
	s_cmp_lt_u32 s101, 16
	s_cbranch_scc1 .LslotA_skip
	s_lshl_b32 s98, s98, 4
	s_add_i32 s98, s98, s101
	s_sub_i32 s98, s98, 16
	s_lshl_b32 s100, s100, 4
	s_add_i32 s98, s98, 0x600
	v_writelane_b32 v253, s14, 0
	v_writelane_b32 v253, s15, 1
	v_writelane_b32 v253, s16, 2
	v_writelane_b32 v253, s17, 3
	v_writelane_b32 v253, s19, 4
	v_writelane_b32 v253, s21, 5
	v_writelane_b32 v253, s57, 6
	v_mov_b32_e32 v254, v3
	s_mov_b32 s99, 5
	s_mov_b32 s101, 0x4100
	s_lshl_b32 s50, s98, 3
	s_add_i32 s50, s50, s85
	s_lshl_b32 s49, s98, 9
	s_lshl_b32 s48, s100, 3
	s_lshl_b32 s2, s100, 9
	s_mov_b64 s[0:1], s[78:79]
	s_mul_i32 s3, s85, 0x4100
	s_lshl_b32 s88, s85, 6
	s_branch .Lconv_entry
.LslotA_ret:
	v_readlane_b32 s14, v253, 0
	v_readlane_b32 s15, v253, 1
	v_readlane_b32 s16, v253, 2
	v_readlane_b32 s17, v253, 3
	v_readlane_b32 s19, v253, 4
	v_readlane_b32 s21, v253, 5
	v_readlane_b32 s57, v253, 6
	v_mov_b32_e32 v3, v254
	s_waitcnt vmcnt(0) lgkmcnt(0)
	s_nop 4

;     __device__ bool next(int i, Unit& u) const {
;         const long L = (long)i * G + c; int wgid;
;         if (aligned) {
;             const int ng = (nM + WGM - 1) / WGM, gq = ng / NXCD, gr = ng % NXCD, xcd = (int)(L % NXCD); const long off = L / NXCD;
;             const int g0 = xcd * gq + (xcd < gr ? xcd : gr), g1 = g0 + gq + (xcd < gr ? 1 : 0);
;             const long w = (long)g0 * (WGM * 4) + off, wend = (long)g1 * (WGM * 4) < nwg ? (long)g1 * (WGM * 4) : nwg;
;             if (w >= wend) return false;
;             wgid = (int)w;
; __global__ void __launch_bounds__(NWAVES * 64, 2) mk_fwd(Args args) {
;     ...
;         {
;             const int step = G * NWAVES; int it0 = CONV_EARLY + bid * NWAVES + wave;
;             ConvDesc dA, dB; f32x4 vA[16], vB[16];
;             if (it0 < NCONV_ITEMS) { CONV_DECODE(dA, it0); conv_load(vA, dA, lane); }
; #pragma unroll 1
;             for (; it0 < NCONV_ITEMS; it0 += 2 * step) {
;                 const bool hasB = it0 + step < NCONV_ITEMS, hasA2 = it0 + 2 * step < NCONV_ITEMS;
;                 if (hasB) { CONV_DECODE(dB, it0 + step); conv_load(vB, dB, lane); }
;                 conv_process(vA, dA, scr, lane);
;                 if (hasA2) { CONV_DECODE(dA, it0 + 2 * step); conv_load(vA, dA, lane); }
;                 if (hasB) conv_process(vB, dB, scr, lane);
;             }
.LBB0_1657:
	s_waitcnt vmcnt(0) lgkmcnt(0)
	s_barrier
	v_mov_b32_e32 v252, 0x27c80
	ds_read_b32 v252, v252
	s_waitcnt lgkmcnt(0)
	v_readfirstlane_b32 s100, v252
	s_nop 1
	s_lshr_b32 s100, s100, 8
	s_add_i32 s100, s100, 3
	s_lshr_b32 s100, s100, 2
	s_and_b32 s100, s100, 7
	s_and_b32 s98, s83, 7
	s_cmp_eq_u32 s100, 0
	s_cbranch_scc1 .Lsp_all
	s_cmp_ge_u32 s100, 6
	s_cbranch_scc1 .Lsp_all
	s_lshr_b32 s101, s83, 3
	s_cmp_lt_u32 s98, s100
	s_cbranch_scc1 .Lsp_heavy
	s_sub_i32 s98, s98, s100
	s_lshl_b32 s98, s98, 5
	s_add_i32 s98, s98, s101
	s_sub_i32 s100, 8, s100
	s_lshl_b32 s100, s100, 5
	s_add_i32 s98, s98, 0x780
	s_branch .Lsp_go
.Lsp_heavy:
	s_cmp_lt_u32 s101, 16
	s_cbranch_scc1 .Lq_done
	s_lshl_b32 s98, s98, 4
	s_add_i32 s98, s98, s101
	s_sub_i32 s98, s98, 16
	s_lshl_b32 s100, s100, 4
	s_add_i32 s98, s98, 0x700
	s_mov_b32 s99, 2
	s_mov_b32 s101, 0x4500
	s_lshl_b32 s50, s98, 3
	s_add_i32 s50, s50, s85
	s_lshl_b32 s49, s98, 9
	s_lshl_b32 s48, s100, 3
	s_lshl_b32 s2, s100, 9
	s_mov_b64 s[0:1], s[78:79]
	s_mul_i32 s3, s85, 0x4100
	s_lshl_b32 s88, s85, 6
	s_branch .Lconv_entry
.Lsp_all:
	s_add_i32 s98, s83, 0x600
	s_mov_b32 s100, s33
.Lsp_go:
	s_mov_b32 s99, 2
	s_mov_b32 s101, 0x6900
	s_lshl_b32 s50, s98, 3
	s_add_i32 s50, s50, s85
	s_lshl_b32 s49, s98, 9
	s_lshl_b32 s48, s100, 3
	s_lshl_b32 s2, s100, 9
	s_mov_b64 s[0:1], s[78:79]
	s_mul_i32 s3, s85, 0x4100
	s_lshl_b32 s88, s85, 6
	s_branch .Lconv_entry
